# v56 + moe1 unit begin: the next unit's four gathered-row offset loads issued together with one wait instead of four load-wait round trips
# speedup vs baseline: 1.0222x; 1.0046x over previous
; #define PG8_AOFFS(dst, U) do { int t2_ = tid; asm volatile("" : "+v"(t2_)); _Pragma("unroll") for (int i = 0; i < 2; ++i) { int R, C; stage_rc(t2_ * 16 + i * 8192, R, C); \
;         dst[0][i] = S.a_off(U, R) + (unsigned)C * 2u; dst[1][i] = S.a_off(U, HALF + R) + (unsigned)C * 2u; } } while (0)
;     __device__ __forceinline__ bool next(int i, Unit& u) const { return o.next(i, u); }
;     __device__ __forceinline__ unsigned a_off(const Unit& u, int r) const { return (unsigned)(u.pm * 256 + r) * (unsigned)(K * 2); }
; template <class Epi, class Sched>
; __device__ __forceinline__ void gemm_phase(LAS unsigned char* lds, const int tid, const char* Abase, const int K, const Sched& S, const Epi& E) {
;     ...
;         const bool has_next = S.next(ui + 1, nxt);
;         const char* nB = cB;
;         { unsigned vn[2][2];
;           if (has_next) { PG8_AOFFS(vn, nxt); nB = S.b_tile(nxt); *vslot = (u32x4){vn[0][0], vn[0][1], vn[1][0], vn[1][1]}; }
;     __device__ __forceinline__ unsigned a_off(const Unit& u, int r) const {
;         if (gather) { int tok = 0; if (r < u.nrows) tok = liste[(size_t)u.e * T + 256 * u.tile + r] >> 1; return (unsigned)tok * (unsigned)(K * 2); }
.LBB0_1178:
	s_or_b64 exec, exec, s[38:39]
	v_add_u32_e32 v147, 0x80, v136
	v_cmp_lt_i32_e32 vcc, v147, v157
	v_mov_b32_e32 v240, 0
	v_mov_b32_e32 v241, 0
	s_and_saveexec_b64 s[38:39], vcc
	s_cbranch_execz .LBB0_1180
	v_lshl_add_u64 v[136:137], v[136:137], 2, v[134:135]
	flat_load_dword v240, v[136:137] offset:512

;     __device__ __forceinline__ unsigned a_off(const Unit& u, int r) const { return (unsigned)(u.pm * 256 + r) * (unsigned)(K * 2); }
;     __device__ __forceinline__ unsigned a_off(const Unit& u, int r) const {
;         if (gather) { int tok = 0; if (r < u.nrows) tok = liste[(size_t)u.e * T + 256 * u.tile + r] >> 1; return (unsigned)tok * (unsigned)(K * 2); }
.LBB0_1182:
	s_or_b64 exec, exec, s[38:39]
	v_add_u32_e32 v151, 0x80, v136
	v_cmp_lt_i32_e32 vcc, v151, v157
	s_and_saveexec_b64 s[38:39], vcc
	s_cbranch_execz .LBB0_1184
	v_lshl_add_u64 v[134:135], v[136:137], 2, v[134:135]
	flat_load_dword v241, v[134:135] offset:512
.LBB0_1184:
	s_or_b64 exec, exec, s[38:39]
	s_waitcnt vmcnt(0) lgkmcnt(0)
	v_lshlrev_b32_e32 v145, 10, v145
	v_lshlrev_b32_e32 v240, 10, v240
	v_lshlrev_b32_e32 v150, 10, v150
	v_lshlrev_b32_e32 v241, 10, v241
	v_and_b32_e32 v145, 0xfffff800, v145
	v_and_b32_e32 v144, 0xfffff800, v240
	v_and_b32_e32 v150, 0xfffff800, v150
	v_and_b32_e32 v148, 0xfffff800, v241
	v_lshlrev_b32_e32 v135, 6, v149
	v_sub_u32_e32 v135, v147, v135
	v_lshlrev_b32_e32 v134, 5, v146
	v_ashrrev_i16_sdwa v135, v235, sext(v135) dst_sel:DWORD dst_unused:UNUSED_PAD src0_sel:DWORD src1_sel:BYTE_0
	v_and_b32_e32 v134, 32, v134
	v_bfe_i32 v135, v135, 0, 16
	v_add_lshl_u32 v137, v134, v135, 1
	v_lshlrev_b32_e32 v134, 6, v143
	s_ashr_i32 s31, s30, 31
	v_sub_u32_e32 v134, v142, v134
	s_lshl_b64 s[6:7], s[30:31], 19
	s_lshl_b64 s[38:39], s[34:35], 20
	v_lshlrev_b32_e32 v0, 5, v0
	v_ashrrev_i16_sdwa v134, v235, sext(v134) dst_sel:DWORD dst_unused:UNUSED_PAD src0_sel:DWORD src1_sel:BYTE_0
	s_add_u32 s3, s46, s38
	v_and_b32_e32 v0, 32, v0
	v_bfe_i32 v134, v134, 0, 16
	s_addc_u32 s31, s47, s39
	v_add_lshl_u32 v0, v0, v134, 1
	s_add_u32 s38, s3, s6
	v_add_u32_e32 v135, v150, v137
	v_add_u32_e32 v136, v144, v0
	v_add_u32_e32 v134, v145, v0
	v_add_u32_e32 v137, v148, v137
	s_addc_u32 s39, s31, s7
